# GEMM1/GEMM2: first K-tile of each unit peeled with C=0 (no accumulator zeroing), on top of v26
# speedup vs baseline: 1.0063x; 1.0017x over previous
;     ...
; #pragma unroll
;         for (int a = 0; a < 2; ++a)
; #pragma unroll
;             for (int b = 0; b < 2; ++b)
; #pragma unroll
;                 for (int m = 0; m < 4; ++m)
; #pragma unroll
;                     for (int n = 0; n < 2; ++n) acc[a][b][m][n] = (f32x4){0.f, 0.f, 0.f, 0.f};
;         cur = nxt; cA = nA; cB = nB; ++ui; tbi = tbn;
.LBB0_990:
	s_lshl_b32 s0, s64, 19
	s_and_b64 s[22:23], s[34:35], exec
	s_cselect_b32 s1, s0, s68
	s_add_i32 s18, s18, 0
	s_add_i32 s18, s18, 0x20000
	v_mov_b32_e32 v34, 0
	v_add3_u32 v180, s18, v171, v172
	v_add3_u32 v181, s18, v173, v174
	s_mov_b32 s70, -2
	s_movk_i32 s71, 0x100
	ds_read_b128 v[2:5], v176
	ds_read_b128 v[6:9], v176 offset:1024
	ds_read_b128 v[10:13], v176 offset:2048
	ds_read_b128 v[14:17], v176 offset:3072
	s_add_i32 s72, s68, s71
	s_cmp_eq_u32 s70, 12
	s_cselect_b64 s[22:23], -1, 0
	s_and_b64 s[18:19], s[22:23], exec
	s_cselect_b32 s72, s1, s72
	s_add_i32 s18, s71, 0xffffff80
	s_mov_b32 m0, s51
	ds_read_b128 v[182:185], v177
	ds_read_b128 v[186:189], v177 offset:1024
	ds_read_b128 v[190:193], v177 offset:2048
	ds_read_b128 v[194:197], v177 offset:3072
	ds_read_b128 v[198:201], v177 offset:4096
	ds_read_b128 v[202:205], v177 offset:5120
	ds_read_b128 v[206:209], v177 offset:6144
	ds_read_b128 v[210:213], v177 offset:7168
	buffer_load_dwordx4 v165, s[12:15], s18 offen lds
	s_mov_b32 m0, s52
	s_nop 0
	buffer_load_dwordx4 v169, s[12:15], s18 offen lds
	s_waitcnt lgkmcnt(8)
	s_barrier
	s_waitcnt lgkmcnt(0)
	s_setprio 1
	s_waitcnt lgkmcnt(6)
	v_mfma_f32_16x16x128_f8f6f4 v[142:145], v[2:9], v[182:189], 0
	v_mfma_f32_16x16x128_f8f6f4 v[134:137], v[10:17], v[182:189], 0
	s_waitcnt lgkmcnt(4)
	v_mfma_f32_16x16x128_f8f6f4 v[126:129], v[2:9], v[190:197], 0
	v_mfma_f32_16x16x128_f8f6f4 v[118:121], v[10:17], v[190:197], 0
	s_waitcnt lgkmcnt(2)
	v_mfma_f32_16x16x128_f8f6f4 v[146:149], v[2:9], v[198:205], 0
	v_mfma_f32_16x16x128_f8f6f4 v[150:153], v[10:17], v[198:205], 0
	s_waitcnt lgkmcnt(0)
	v_mfma_f32_16x16x128_f8f6f4 v[154:157], v[2:9], v[206:213], 0
	v_mfma_f32_16x16x128_f8f6f4 v[158:161], v[10:17], v[206:213], 0
	s_setprio 0
	s_barrier
	s_mov_b32 s18, s14
	s_mov_b32 s19, s15
	s_mov_b32 m0, s33
	s_nop 1
	ds_read_b128 v[18:21], v178
	ds_read_b128 v[22:25], v178 offset:1024
	ds_read_b128 v[26:29], v178 offset:2048
	ds_read_b128 v[30:33], v178 offset:3072
	buffer_load_dwordx4 v166, s[16:19], s72 offen lds
	s_mov_b32 m0, s36
	s_nop 0
	buffer_load_dwordx4 v168, s[16:19], s72 offen lds
	s_barrier
	s_waitcnt lgkmcnt(0)
	s_setprio 1
	s_waitcnt lgkmcnt(2)
	v_mfma_f32_16x16x128_f8f6f4 v[138:141], v[18:25], v[182:189], 0
	s_and_b64 s[74:75], s[34:35], s[22:23]
	s_waitcnt lgkmcnt(0)
	v_mfma_f32_16x16x128_f8f6f4 v[130:133], v[26:33], v[182:189], 0
	v_mfma_f32_16x16x128_f8f6f4 v[122:125], v[18:25], v[190:197], 0
	v_mfma_f32_16x16x128_f8f6f4 v[114:117], v[26:33], v[190:197], 0
	v_mfma_f32_16x16x128_f8f6f4 v[110:113], v[18:25], v[198:205], 0
	v_mfma_f32_16x16x128_f8f6f4 v[106:109], v[26:33], v[198:205], 0
	v_mfma_f32_16x16x128_f8f6f4 v[102:105], v[18:25], v[206:213], 0
	v_mfma_f32_16x16x128_f8f6f4 v[98:101], v[26:33], v[206:213], 0
	s_setprio 0
	s_andn2_b64 vcc, exec, s[74:75]
	s_barrier
	s_or_b32 s73, s72, 0x80
	s_and_b64 s[22:23], s[22:23], exec
	s_mov_b32 m0, s29
	s_cselect_b32 s22, 0, s71
	ds_read_b128 v[182:185], v177 offset:16384
	ds_read_b128 v[186:189], v177 offset:17408
	ds_read_b128 v[190:193], v177 offset:18432
	ds_read_b128 v[194:197], v177 offset:19456
	ds_read_b128 v[198:201], v177 offset:20480
	ds_read_b128 v[202:205], v177 offset:21504
	ds_read_b128 v[206:209], v177 offset:22528
	ds_read_b128 v[210:213], v177 offset:23552
	buffer_load_dwordx4 v164, s[12:15], s22 offen lds
	s_mov_b32 m0, s37
	s_or_b32 s23, s22, 0x80
	buffer_load_dwordx4 v167, s[12:15], s22 offen lds
	s_barrier
	s_waitcnt lgkmcnt(0)
	s_setprio 1
	s_waitcnt lgkmcnt(6)
	v_mfma_f32_16x16x128_f8f6f4 v[94:97], v[2:9], v[182:189], 0
	v_mfma_f32_16x16x128_f8f6f4 v[86:89], v[10:17], v[182:189], 0
	s_waitcnt lgkmcnt(4)
	v_mfma_f32_16x16x128_f8f6f4 v[78:81], v[2:9], v[190:197], 0
	v_mfma_f32_16x16x128_f8f6f4 v[70:73], v[10:17], v[190:197], 0
	s_waitcnt lgkmcnt(2)
	v_mfma_f32_16x16x128_f8f6f4 v[214:217], v[2:9], v[198:205], 0
	v_mfma_f32_16x16x128_f8f6f4 v[218:221], v[10:17], v[198:205], 0
	s_waitcnt lgkmcnt(0)
	v_mfma_f32_16x16x128_f8f6f4 v[222:225], v[2:9], v[206:213], 0
	v_mfma_f32_16x16x128_f8f6f4 v[226:229], v[10:17], v[206:213], 0
	s_setprio 0
	s_barrier
	s_add_i32 s74, s72, 0x40000
	s_mov_b32 m0, s38
	s_nop 0
	buffer_load_dwordx4 v166, s[16:19], s74 offen lds
	s_mov_b32 m0, s39
	s_nop 0
	buffer_load_dwordx4 v168, s[16:19], s74 offen lds
	s_waitcnt vmcnt(6)
	s_barrier
	s_setprio 1
	v_mfma_f32_16x16x128_f8f6f4 v[90:93], v[18:25], v[182:189], 0
	v_mfma_f32_16x16x128_f8f6f4 v[82:85], v[26:33], v[182:189], 0
	v_mfma_f32_16x16x128_f8f6f4 v[74:77], v[18:25], v[190:197], 0
	v_mfma_f32_16x16x128_f8f6f4 v[66:69], v[26:33], v[190:197], 0
	v_mfma_f32_16x16x128_f8f6f4 v[230:233], v[18:25], v[198:205], 0
	v_mfma_f32_16x16x128_f8f6f4 v[234:237], v[26:33], v[198:205], 0
	v_mfma_f32_16x16x128_f8f6f4 v[238:241], v[18:25], v[206:213], 0
	v_mfma_f32_16x16x128_f8f6f4 v[242:245], v[26:33], v[206:213], 0
	s_setprio 0
	v_add_u32_e32 v14, 0x18000, v175
	s_barrier
	s_branch .Lmid_g1

.Lmid_g1:
	ds_read_b128 v[2:5], v14
	ds_read_b128 v[6:9], v14 offset:1024
	ds_read_b128 v[10:13], v14 offset:2048
	ds_read_b128 v[14:17], v14 offset:3072
	s_mov_b32 m0, s40
	ds_read_b128 v[34:37], v177 offset:32768
	ds_read_b128 v[38:41], v177 offset:33792
	ds_read_b128 v[42:45], v177 offset:34816
	ds_read_b128 v[46:49], v177 offset:35840
	ds_read_b128 v[50:53], v177 offset:36864
	ds_read_b128 v[54:57], v177 offset:37888
	ds_read_b128 v[58:61], v177 offset:38912
	ds_read_b128 v[62:65], v177 offset:39936
	buffer_load_dwordx4 v165, s[12:15], s22 offen lds
	s_mov_b32 m0, s41
	s_nop 0
	buffer_load_dwordx4 v169, s[12:15], s22 offen lds
	s_waitcnt lgkmcnt(8)
	s_barrier
	s_waitcnt lgkmcnt(0)
	s_setprio 1
	s_waitcnt lgkmcnt(6)
	v_mfma_f32_16x16x128_f8f6f4 v[142:145], v[2:9], v[34:41], v[142:145]
	v_mfma_f32_16x16x128_f8f6f4 v[134:137], v[10:17], v[34:41], v[134:137]
	s_waitcnt lgkmcnt(4)
	v_mfma_f32_16x16x128_f8f6f4 v[126:129], v[2:9], v[42:49], v[126:129]
	v_mfma_f32_16x16x128_f8f6f4 v[118:121], v[10:17], v[42:49], v[118:121]
	s_waitcnt lgkmcnt(2)
	v_mfma_f32_16x16x128_f8f6f4 v[30:33], v[2:9], v[50:57], v[146:149]
	v_mfma_f32_16x16x128_f8f6f4 v[26:29], v[10:17], v[50:57], v[150:153]
	s_waitcnt lgkmcnt(0)
	v_mfma_f32_16x16x128_f8f6f4 v[22:25], v[2:9], v[58:65], v[154:157]
	v_mfma_f32_16x16x128_f8f6f4 v[18:21], v[10:17], v[58:65], v[158:161]
	s_setprio 0
	s_barrier
	s_nop 4
	v_add_u32_e32 v158, 0x1c000, v175
	s_mov_b32 m0, s45
	ds_read_b128 v[146:149], v158
	ds_read_b128 v[150:153], v158 offset:1024
	ds_read_b128 v[154:157], v158 offset:2048
	ds_read_b128 v[158:161], v158 offset:3072
	buffer_load_dwordx4 v166, s[16:19], s73 offen lds
	s_mov_b32 m0, s46
	s_nop 0
	buffer_load_dwordx4 v168, s[16:19], s73 offen lds
	s_barrier
	s_waitcnt lgkmcnt(0)
	s_setprio 1
	s_waitcnt lgkmcnt(2)
	v_mfma_f32_16x16x128_f8f6f4 v[138:141], v[146:153], v[34:41], v[138:141]
	s_waitcnt lgkmcnt(0)
	v_mfma_f32_16x16x128_f8f6f4 v[130:133], v[154:161], v[34:41], v[130:133]
	v_mfma_f32_16x16x128_f8f6f4 v[122:125], v[146:153], v[42:49], v[122:125]
	v_mfma_f32_16x16x128_f8f6f4 v[114:117], v[154:161], v[42:49], v[114:117]
	v_mfma_f32_16x16x128_f8f6f4 v[110:113], v[146:153], v[50:57], v[110:113]
	v_mfma_f32_16x16x128_f8f6f4 v[106:109], v[154:161], v[50:57], v[106:109]
	v_mfma_f32_16x16x128_f8f6f4 v[102:105], v[146:153], v[58:65], v[102:105]
	v_mfma_f32_16x16x128_f8f6f4 v[98:101], v[154:161], v[58:65], v[98:101]
	s_setprio 0
	s_mov_b32 m0, s47
	s_barrier
	ds_read_b128 v[182:185], v177 offset:49152
	ds_read_b128 v[186:189], v177 offset:50176
	ds_read_b128 v[190:193], v177 offset:51200
	ds_read_b128 v[194:197], v177 offset:52224
	ds_read_b128 v[198:201], v177 offset:53248
	ds_read_b128 v[202:205], v177 offset:54272
	ds_read_b128 v[206:209], v177 offset:55296
	ds_read_b128 v[210:213], v177 offset:56320
	buffer_load_dwordx4 v164, s[12:15], s23 offen lds
	s_mov_b32 m0, s48
	s_nop 0
	buffer_load_dwordx4 v167, s[12:15], s23 offen lds
	s_barrier
	s_waitcnt lgkmcnt(0)
	s_setprio 1
	s_waitcnt lgkmcnt(6)
	v_mfma_f32_16x16x128_f8f6f4 v[94:97], v[2:9], v[182:189], v[94:97]
	v_mfma_f32_16x16x128_f8f6f4 v[86:89], v[10:17], v[182:189], v[86:89]
	s_waitcnt lgkmcnt(4)
	v_mfma_f32_16x16x128_f8f6f4 v[78:81], v[2:9], v[190:197], v[78:81]
	v_mfma_f32_16x16x128_f8f6f4 v[70:73], v[10:17], v[190:197], v[70:73]
	s_waitcnt lgkmcnt(2)
	v_mfma_f32_16x16x128_f8f6f4 v[62:65], v[2:9], v[198:205], v[214:217]
	v_mfma_f32_16x16x128_f8f6f4 v[54:57], v[10:17], v[198:205], v[218:221]
	s_waitcnt lgkmcnt(0)
	v_mfma_f32_16x16x128_f8f6f4 v[46:49], v[2:9], v[206:213], v[222:225]
	v_mfma_f32_16x16x128_f8f6f4 v[38:41], v[10:17], v[206:213], v[226:229]
	s_setprio 0
	s_barrier
	s_add_i32 s72, s72, 0x40080
	s_mov_b32 m0, s49
	s_nop 0
	buffer_load_dwordx4 v166, s[16:19], s72 offen lds
	s_mov_b32 m0, s50
	s_nop 0
	buffer_load_dwordx4 v168, s[16:19], s72 offen lds
	s_waitcnt vmcnt(6)
	s_barrier
	s_setprio 1
	v_mfma_f32_16x16x128_f8f6f4 v[90:93], v[146:153], v[182:189], v[90:93]
	v_mfma_f32_16x16x128_f8f6f4 v[82:85], v[154:161], v[182:189], v[82:85]
	v_mfma_f32_16x16x128_f8f6f4 v[74:77], v[146:153], v[190:197], v[74:77]
	v_mfma_f32_16x16x128_f8f6f4 v[66:69], v[154:161], v[190:197], v[66:69]
	v_mfma_f32_16x16x128_f8f6f4 v[58:61], v[146:153], v[198:205], v[230:233]
	v_mfma_f32_16x16x128_f8f6f4 v[50:53], v[154:161], v[198:205], v[234:237]
	v_mfma_f32_16x16x128_f8f6f4 v[42:45], v[146:153], v[206:213], v[238:241]
	v_mfma_f32_16x16x128_f8f6f4 v[34:37], v[154:161], v[206:213], v[242:245]
	s_setprio 0
	s_add_i32 s70, s70, 2
	s_addk_i32 s71, 0x100
	s_cmp_gt_u32 s70, 13
	s_barrier
	s_cbranch_scc1 .LBB0_979

;     ...
; #pragma unroll
;         for (int a = 0; a < 2; ++a)
; #pragma unroll
;             for (int b = 0; b < 2; ++b)
; #pragma unroll
;                 for (int m = 0; m < 4; ++m)
; #pragma unroll
;                     for (int n = 0; n < 2; ++n) acc[a][b][m][n] = (f32x4){0.f, 0.f, 0.f, 0.f};
;         cur = nxt; cA = nA; cB = nB; ++ui; tbi = tbn;
.LBB0_1080:
	s_lshl_b32 s10, s60, 19
	s_and_b64 s[18:19], s[0:1], exec
	s_cselect_b32 s18, s10, s67
	s_lshl_b32 s11, s62, 19
	s_and_b64 s[0:1], s[0:1], exec
	v_mov_b32_e32 v26, 0
	s_cselect_b32 s0, s11, s66
	s_add_i32 s1, s67, 0x40080
	s_add_i32 s19, s66, 0x100
	s_mov_b32 s66, -2
	s_waitcnt lgkmcnt(0)
	ds_read_b128 v[126:129], v153
	ds_read_b128 v[130:133], v153 offset:1024
	ds_read_b128 v[138:141], v153 offset:2048
	ds_read_b128 v[142:145], v153 offset:3072
	s_add_i32 s26, s1, 0xfffc0080
	s_cmp_eq_u32 s66, 12
	s_cselect_b32 s69, s18, s26
	s_cselect_b32 s67, s0, s19
	s_or_b32 s68, s69, 0x80
	s_mov_b32 m0, s51
	ds_read_b128 v[160:163], v154
	ds_read_b128 v[164:167], v154 offset:1024
	ds_read_b128 v[168:171], v154 offset:2048
	ds_read_b128 v[172:175], v154 offset:3072
	ds_read_b128 v[176:179], v154 offset:4096
	ds_read_b128 v[180:183], v154 offset:5120
	ds_read_b128 v[184:187], v154 offset:6144
	ds_read_b128 v[188:191], v154 offset:7168
	buffer_load_dwordx4 v1, s[20:23], s1 offen lds
	s_mov_b32 m0, s52
	s_nop 0
	buffer_load_dwordx4 v252, s[20:23], s1 offen lds
	s_waitcnt lgkmcnt(8)
	s_barrier
	s_waitcnt lgkmcnt(0)
	s_setprio 1
	s_waitcnt lgkmcnt(6)
	v_mfma_f32_16x16x128_f8f6f4 v[134:137], v[126:133], v[160:167], 0
	v_mfma_f32_16x16x128_f8f6f4 v[122:125], v[138:145], v[160:167], 0
	s_waitcnt lgkmcnt(4)
	v_mfma_f32_16x16x128_f8f6f4 v[192:195], v[126:133], v[168:175], 0
	v_mfma_f32_16x16x128_f8f6f4 v[196:199], v[138:145], v[168:175], 0
	s_waitcnt lgkmcnt(2)
	v_mfma_f32_16x16x128_f8f6f4 v[200:203], v[126:133], v[176:183], 0
	v_mfma_f32_16x16x128_f8f6f4 v[204:207], v[138:145], v[176:183], 0
	s_waitcnt lgkmcnt(0)
	v_mfma_f32_16x16x128_f8f6f4 v[208:211], v[126:133], v[184:191], 0
	v_mfma_f32_16x16x128_f8f6f4 v[212:215], v[138:145], v[184:191], 0
	s_setprio 0
	s_barrier
	s_mov_b32 s26, s22
	s_mov_b32 s27, s23
	s_mov_b32 m0, s36
	s_nop 1
	ds_read_b128 v[74:77], v155
	ds_read_b128 v[78:81], v155 offset:1024
	ds_read_b128 v[90:93], v155 offset:2048
	ds_read_b128 v[94:97], v155 offset:3072
	buffer_load_dwordx4 v253, s[24:27], s67 offen lds
	s_mov_b32 m0, s37
	s_nop 0
	buffer_load_dwordx4 v150, s[24:27], s67 offen lds
	s_barrier
	s_waitcnt lgkmcnt(0)
	s_setprio 1
	s_waitcnt lgkmcnt(2)
	v_mfma_f32_16x16x128_f8f6f4 v[118:121], v[74:81], v[160:167], 0
	s_waitcnt lgkmcnt(0)
	v_mfma_f32_16x16x128_f8f6f4 v[114:117], v[90:97], v[160:167], 0
	v_mfma_f32_16x16x128_f8f6f4 v[160:163], v[74:81], v[168:175], 0
	v_mfma_f32_16x16x128_f8f6f4 v[164:167], v[90:97], v[168:175], 0
	v_mfma_f32_16x16x128_f8f6f4 v[168:171], v[74:81], v[176:183], 0
	v_mfma_f32_16x16x128_f8f6f4 v[172:175], v[90:97], v[176:183], 0
	v_mfma_f32_16x16x128_f8f6f4 v[176:179], v[74:81], v[184:191], 0
	v_mfma_f32_16x16x128_f8f6f4 v[180:183], v[90:97], v[184:191], 0
	s_setprio 0
	s_mov_b32 m0, s35
	s_barrier
	s_nop 3
	ds_read_b128 v[66:69], v154 offset:16384
	ds_read_b128 v[70:73], v154 offset:17408
	ds_read_b128 v[82:85], v154 offset:18432
	ds_read_b128 v[86:89], v154 offset:19456
	ds_read_b128 v[98:101], v154 offset:20480
	ds_read_b128 v[102:105], v154 offset:21504
	ds_read_b128 v[106:109], v154 offset:22528
	ds_read_b128 v[110:113], v154 offset:23552
	buffer_load_dwordx4 v1, s[20:23], s69 offen lds
	s_mov_b32 m0, s38
	s_nop 0
	buffer_load_dwordx4 v252, s[20:23], s69 offen lds
	s_barrier
	s_waitcnt lgkmcnt(0)
	s_setprio 1
	s_waitcnt lgkmcnt(6)
	v_mfma_f32_16x16x128_f8f6f4 v[62:65], v[126:133], v[66:73], 0
	v_mfma_f32_16x16x128_f8f6f4 v[58:61], v[138:145], v[66:73], 0
	s_waitcnt lgkmcnt(4)
	v_mfma_f32_16x16x128_f8f6f4 v[184:187], v[126:133], v[82:89], 0
	v_mfma_f32_16x16x128_f8f6f4 v[188:191], v[138:145], v[82:89], 0
	s_waitcnt lgkmcnt(2)
	v_mfma_f32_16x16x128_f8f6f4 v[216:219], v[126:133], v[98:105], 0
	v_mfma_f32_16x16x128_f8f6f4 v[220:223], v[138:145], v[98:105], 0
	s_waitcnt lgkmcnt(0)
	v_mfma_f32_16x16x128_f8f6f4 v[224:227], v[126:133], v[106:113], 0
	v_mfma_f32_16x16x128_f8f6f4 v[228:231], v[138:145], v[106:113], 0
	s_setprio 0
	s_barrier
	s_add_i32 s70, s67, 0x40000
	s_mov_b32 m0, s39
	s_nop 0
	buffer_load_dwordx4 v253, s[24:27], s70 offen lds
	s_mov_b32 m0, s40
	s_nop 0
	buffer_load_dwordx4 v150, s[24:27], s70 offen lds
	s_waitcnt vmcnt(6)
	s_barrier
	s_setprio 1
	v_mfma_f32_16x16x128_f8f6f4 v[54:57], v[74:81], v[66:73], 0
	v_mfma_f32_16x16x128_f8f6f4 v[50:53], v[90:97], v[66:73], 0
	v_mfma_f32_16x16x128_f8f6f4 v[232:235], v[74:81], v[82:89], 0
	v_mfma_f32_16x16x128_f8f6f4 v[236:239], v[90:97], v[82:89], 0
	v_mfma_f32_16x16x128_f8f6f4 v[240:243], v[74:81], v[98:105], 0
	v_mfma_f32_16x16x128_f8f6f4 v[244:247], v[90:97], v[98:105], 0
	v_mfma_f32_16x16x128_f8f6f4 v[248:251], v[74:81], v[106:113], 0
	v_mfma_f32_16x16x128_f8f6f4 v[146:149], v[90:97], v[106:113], 0
	s_setprio 0
	s_barrier
	s_branch .Lmid_g2

.Lmid_g2:
	ds_read_b128 v[2:5], v156
	ds_read_b128 v[6:9], v156 offset:1024
	s_nop 2
	ds_read_b128 v[10:13], v156 offset:2048
	ds_read_b128 v[14:17], v156 offset:3072
	s_add_i32 s69, s69, 0x40000
	s_mov_b32 m0, s41
	ds_read_b128 v[18:21], v154 offset:32768
	ds_read_b128 v[22:25], v154 offset:33792
	ds_read_b128 v[26:29], v154 offset:34816
	ds_read_b128 v[30:33], v154 offset:35840
	ds_read_b128 v[34:37], v154 offset:36864
	ds_read_b128 v[38:41], v154 offset:37888
	ds_read_b128 v[42:45], v154 offset:38912
	ds_read_b128 v[46:49], v154 offset:39936
	buffer_load_dwordx4 v1, s[20:23], s69 offen lds
	s_mov_b32 m0, s42
	s_nop 0
	buffer_load_dwordx4 v252, s[20:23], s69 offen lds
	s_waitcnt lgkmcnt(8)
	s_barrier
	s_waitcnt lgkmcnt(0)
	s_setprio 1
	s_waitcnt lgkmcnt(6)
	v_mfma_f32_16x16x128_f8f6f4 v[134:137], v[2:9], v[18:25], v[134:137]
	v_mfma_f32_16x16x128_f8f6f4 v[122:125], v[10:17], v[18:25], v[122:125]
	s_waitcnt lgkmcnt(4)
	v_mfma_f32_16x16x128_f8f6f4 v[110:113], v[2:9], v[26:33], v[192:195]
	v_mfma_f32_16x16x128_f8f6f4 v[106:109], v[10:17], v[26:33], v[196:199]
	s_waitcnt lgkmcnt(2)
	v_mfma_f32_16x16x128_f8f6f4 v[94:97], v[2:9], v[34:41], v[200:203]
	v_mfma_f32_16x16x128_f8f6f4 v[90:93], v[10:17], v[34:41], v[204:207]
	s_waitcnt lgkmcnt(0)
	v_mfma_f32_16x16x128_f8f6f4 v[78:81], v[2:9], v[42:49], v[208:211]
	v_mfma_f32_16x16x128_f8f6f4 v[74:77], v[10:17], v[42:49], v[212:215]
	s_setprio 0
	s_barrier
	s_add_i32 s69, s67, 0x80
	s_mov_b32 m0, s45
	ds_read_b128 v[126:129], v157
	ds_read_b128 v[130:133], v157 offset:1024
	ds_read_b128 v[138:141], v157 offset:2048
	ds_read_b128 v[142:145], v157 offset:3072
	buffer_load_dwordx4 v253, s[24:27], s69 offen lds
	s_mov_b32 m0, s46
	s_nop 0
	buffer_load_dwordx4 v150, s[24:27], s69 offen lds
	s_barrier
	s_waitcnt lgkmcnt(0)
	s_setprio 1
	s_waitcnt lgkmcnt(2)
	v_mfma_f32_16x16x128_f8f6f4 v[118:121], v[126:133], v[18:25], v[118:121]
	s_waitcnt lgkmcnt(0)
	v_mfma_f32_16x16x128_f8f6f4 v[114:117], v[138:145], v[18:25], v[114:117]
	v_mfma_f32_16x16x128_f8f6f4 v[102:105], v[126:133], v[26:33], v[160:163]
	v_mfma_f32_16x16x128_f8f6f4 v[98:101], v[138:145], v[26:33], v[164:167]
	v_mfma_f32_16x16x128_f8f6f4 v[86:89], v[126:133], v[34:41], v[168:171]
	v_mfma_f32_16x16x128_f8f6f4 v[82:85], v[138:145], v[34:41], v[172:175]
	v_mfma_f32_16x16x128_f8f6f4 v[70:73], v[126:133], v[42:49], v[176:179]
	v_mfma_f32_16x16x128_f8f6f4 v[66:69], v[138:145], v[42:49], v[180:183]
	s_setprio 0
	s_mov_b32 m0, s47
	s_barrier
	ds_read_b128 v[26:29], v154 offset:49152
	ds_read_b128 v[30:33], v154 offset:50176
	ds_read_b128 v[34:37], v154 offset:51200
	ds_read_b128 v[38:41], v154 offset:52224
	ds_read_b128 v[160:163], v154 offset:53248
	ds_read_b128 v[164:167], v154 offset:54272
	ds_read_b128 v[168:171], v154 offset:55296
	ds_read_b128 v[172:175], v154 offset:56320
	buffer_load_dwordx4 v1, s[20:23], s68 offen lds
	s_mov_b32 m0, s48
	s_nop 0
	buffer_load_dwordx4 v252, s[20:23], s68 offen lds
	s_barrier
	s_waitcnt lgkmcnt(0)
	s_setprio 1
	s_waitcnt lgkmcnt(6)
	v_mfma_f32_16x16x128_f8f6f4 v[62:65], v[2:9], v[26:33], v[62:65]
	v_mfma_f32_16x16x128_f8f6f4 v[58:61], v[10:17], v[26:33], v[58:61]
	s_waitcnt lgkmcnt(4)
	v_mfma_f32_16x16x128_f8f6f4 v[46:49], v[2:9], v[34:41], v[184:187]
	v_mfma_f32_16x16x128_f8f6f4 v[42:45], v[10:17], v[34:41], v[188:191]
	s_waitcnt lgkmcnt(2)
	v_mfma_f32_16x16x128_f8f6f4 v[22:25], v[2:9], v[160:167], v[216:219]
	v_mfma_f32_16x16x128_f8f6f4 v[18:21], v[10:17], v[160:167], v[220:223]
	s_waitcnt lgkmcnt(0)
	v_mfma_f32_16x16x128_f8f6f4 v[6:9], v[2:9], v[168:175], v[224:227]
	v_mfma_f32_16x16x128_f8f6f4 v[2:5], v[10:17], v[168:175], v[228:231]
	s_setprio 0
	s_barrier
	s_add_i32 s67, s67, 0x40080
	s_mov_b32 m0, s49
	s_nop 0
	buffer_load_dwordx4 v253, s[24:27], s67 offen lds
	s_mov_b32 m0, s50
	s_nop 0
	buffer_load_dwordx4 v150, s[24:27], s67 offen lds
	s_waitcnt vmcnt(6)
	s_barrier
; #define LAS __attribute__((address_space(3)))
;     __device__ __forceinline__ void operator()(const f32x4 (&acc)[2][2][4][2], const Unit& u, int wr, int wc, int fr, int fq, LAS const unsigned char* tbl, LAS const unsigned char* b2l) const {
;         { int t_ = threadIdx.x; asm volatile("" : "+v"(t_)); fr = t_ & 15; fq = (t_ >> 4) & 3; }
;         const int r0 = wr * 64 + fr; const int col0 = u.pn * BM + wc * 32 + 8 * fq;
;         unsigned char* Y = ws + WS_Y;
;         f32x4 bv[2][2];
; #pragma unroll
;         for (int bj = 0; bj < 2; ++bj)
; #pragma unroll
;             for (int n = 0; n < 2; ++n) bv[bj][n] = *(LAS const f32x4*)(b2l + (wc * 32 + 8 * fq + bj * HALF + 4 * n) * 4);
; #pragma unroll
;         for (int ai = 0; ai < 2; ++ai)
; #pragma unroll
;             for (int m = 0; m < 4; ++m) { const int row = r0 + ai * HALF + m * 16;
;                 if (u.pos0 + row < u.cnt) { const int pid = *(LAS const int*)(tbl + row * 4); const float gt = *(LAS const float*)(tbl + 1024 + row * 4) * Y_FP8_SCALE; unsigned char* rowp = Y + (size_t)pid * D_ + col0;
; #pragma unroll
;                     for (int bj = 0; bj < 2; ++bj) { const f32x4 v0 = (acc[ai][bj][m][0] * (1.0f / W_FP8_SCALE) + bv[bj][0]) * gt, v1 = (acc[ai][bj][m][1] * (1.0f / W_FP8_SCALE) + bv[bj][1]) * gt;
;                         u32x2 w; w.x = pk4_fp8(v0[0], v0[1], v0[2], v0[3]); w.y = pk4_fp8(v1[0], v1[1], v1[2], v1[3]);
;                         *(u32x2*)(rowp + bj * HALF) = w; } } }
;     ...
;         if (FP8 == 2) { for (int t = 0; t < 8; t += 2) PG8_ITER(false); for (int t = 8; t < nt; t += 2) PG8_ITER(true); }
;         else { for (int t = 0; t < nt; t += 2) PG8_ITER(FP8 == 1); }
;     ...
;         E(acc, cur, wr, wc, fr, fq, lds + STAGE_BYTES + tbi * 2048, lds + PG8_B2L(tbi)); S.done(cur);
	s_setprio 1
	v_mfma_f32_16x16x128_f8f6f4 v[54:57], v[126:133], v[26:33], v[54:57]
	v_mfma_f32_16x16x128_f8f6f4 v[50:53], v[138:145], v[26:33], v[50:53]
	v_mfma_f32_16x16x128_f8f6f4 v[30:33], v[126:133], v[34:41], v[232:235]
	v_mfma_f32_16x16x128_f8f6f4 v[26:29], v[138:145], v[34:41], v[236:239]
	v_mfma_f32_16x16x128_f8f6f4 v[38:41], v[126:133], v[160:167], v[240:243]
	v_mfma_f32_16x16x128_f8f6f4 v[34:37], v[138:145], v[160:167], v[244:247]
	v_mfma_f32_16x16x128_f8f6f4 v[14:17], v[126:133], v[168:175], v[248:251]
	v_mfma_f32_16x16x128_f8f6f4 v[10:13], v[138:145], v[168:175], v[146:149]
	s_setprio 0
	s_add_i32 s66, s66, 2
	s_addk_i32 s1, 0x100
	s_addk_i32 s19, 0x100
	s_cmp_gt_u32 s66, 13
	s_barrier
	s_cbranch_scc0 .LBB0_1081
	s_lshl_b32 s0, s65, 11
	s_add_i32 s18, s0, 0
	s_lshl_b32 s0, s65, 10
	s_add_i32 s18, s18, 0x20000
	s_add_i32 s0, s0, 0x21800
	v_mov_b32_e32 v146, v0
	s_cmp_lt_i32 s65, 2
	s_cselect_b32 s0, s0, 0x23800
	v_lshrrev_b32_e32 v126, 1, v146
	v_and_b32_e32 v147, 24, v126
	s_add_i32 s0, s0, 0
	v_or_b32_e32 v126, s44, v147
	v_lshl_add_u32 v126, v126, 2, s0
	ds_read_b128 v[142:145], v126
	ds_read_b128 v[138:141], v126 offset:16
	ds_read_b128 v[130:133], v126 offset:512
	ds_read_b128 v[126:129], v126 offset:528
	s_lshl_b32 s0, s64, 8
	s_or_b32 s0, s0, s44
	v_and_or_b32 v159, v146, 15, s43
	v_or_b32_e32 v146, s0, v147
	v_ashrrev_i32_e32 v147, 31, v146
	v_add_u32_e32 v148, s34, v159
	v_lshl_add_u64 v[146:147], s[6:7], 0, v[146:147]
	v_cmp_gt_i32_e32 vcc, s33, v148
	s_and_saveexec_b64 s[0:1], vcc
	s_cbranch_execz .LBB0_1084
	v_lshl_add_u32 v148, v159, 2, s18
	ds_read2st64_b32 v[148:149], v148 offset1:4
	s_waitcnt lgkmcnt(4)
	v_pk_fma_f32 v[134:135], v[134:135], s[28:29], v[142:143] op_sel_hi:[1,0,1]
	v_pk_fma_f32 v[136:137], v[136:137], s[28:29], v[144:145] op_sel_hi:[1,0,1]
	s_waitcnt lgkmcnt(3)
	v_pk_fma_f32 v[124:125], v[124:125], s[28:29], v[140:141] op_sel_hi:[1,0,1]
	v_pk_fma_f32 v[122:123], v[122:123], s[28:29], v[138:139] op_sel_hi:[1,0,1]
	s_waitcnt lgkmcnt(0)
	v_ashrrev_i32_e32 v161, 31, v148
	v_mov_b32_e32 v160, v148
	v_mul_f32_e32 v148, 0x41800000, v149
	v_pk_mul_f32 v[134:135], v[134:135], v[148:149] op_sel_hi:[1,0]
	v_pk_mul_f32 v[136:137], v[136:137], v[148:149] op_sel_hi:[1,0]
	v_pk_mul_f32 v[124:125], v[124:125], v[148:149] op_sel_hi:[1,0]
	v_pk_mul_f32 v[122:123], v[122:123], v[148:149] op_sel_hi:[1,0]
	v_med3_f32 v149, v134, s55, v158
	v_med3_f32 v135, v135, s55, v158
	v_mov_b32_e32 v134, 0
	v_cvt_pk_fp8_f32 v134, v149, v135
	v_med3_f32 v122, v122, s55, v158
	v_med3_f32 v123, v123, s55, v158
	v_mov_b32_e32 v135, 0
	v_cvt_pk_fp8_f32 v135, v122, v123
	v_pk_fma_f32 v[118:119], v[118:119], s[28:29], v[130:131] op_sel_hi:[1,0,1]
	v_med3_f32 v122, v124, s55, v158
	v_med3_f32 v123, v125, s55, v158
	v_pk_mul_f32 v[118:119], v[118:119], v[148:149] op_sel_hi:[1,0]
	v_pk_fma_f32 v[114:115], v[114:115], s[28:29], v[126:127] op_sel_hi:[1,0,1]
	v_cvt_pk_fp8_f32 v135, v122, v123 op_sel:[0,0,1]
	v_pk_mul_f32 v[114:115], v[114:115], v[148:149] op_sel_hi:[1,0]
	v_med3_f32 v122, v118, s55, v158
	v_med3_f32 v119, v119, s55, v158
	v_mov_b32_e32 v118, 0
	v_cvt_pk_fp8_f32 v118, v122, v119
	v_med3_f32 v114, v114, s55, v158
	v_med3_f32 v115, v115, s55, v158
	v_mov_b32_e32 v119, 0
	v_cvt_pk_fp8_f32 v119, v114, v115
	v_pk_fma_f32 v[120:121], v[120:121], s[28:29], v[132:133] op_sel_hi:[1,0,1]
	v_pk_fma_f32 v[116:117], v[116:117], s[28:29], v[128:129] op_sel_hi:[1,0,1]
	v_med3_f32 v136, v136, s55, v158
	v_med3_f32 v137, v137, s55, v158
	v_pk_mul_f32 v[120:121], v[120:121], v[148:149] op_sel_hi:[1,0]
	v_pk_mul_f32 v[116:117], v[116:117], v[148:149] op_sel_hi:[1,0]
	v_cvt_pk_fp8_f32 v134, v136, v137 op_sel:[0,0,1]
	v_med3_f32 v120, v120, s55, v158
	v_med3_f32 v121, v121, s55, v158
	v_med3_f32 v114, v116, s55, v158
	v_med3_f32 v115, v117, s55, v158
	v_cvt_pk_fp8_f32 v118, v120, v121 op_sel:[0,0,1]
	v_cvt_pk_fp8_f32 v119, v114, v115 op_sel:[0,0,1]
	v_lshlrev_b64 v[114:115], 11, v[160:161]
	v_lshl_add_u64 v[114:115], v[146:147], 0, v[114:115]
	global_store_dwordx2 v[114:115], v[134:135], off
	global_store_dwordx2 v[114:115], v[118:119], off offset:128
